# baseline (speedup 1.0000x reference)
.Lq_dma_loop:
	s_lshl_b32 s40, s38, 10
	s_add_u32 s42, s36, s40
	s_addc_u32 s43, s37, 0
	s_add_i32 s41, s40, 69680
	v_lshl_add_u64 v[114:115], s[42:43], 0, v[116:117]
	s_mov_b32 m0, s41
	s_add_i32 s38, s38, 14
	global_load_lds_dwordx4 v[114:115], off
	s_cmp_lt_u32 s38, 44
	s_cbranch_scc1 .Lq_dma_loop

.LBB1_4:
	s_or_b64 exec, exec, s[4:5]
	v_cmp_eq_u32_e64 s[4:5], 0, v0
	s_and_saveexec_b64 s[6:7], s[4:5]
	v_mov_b32_e32 v1, 0
	v_mov_b32_e32 v2, 0x10408
	ds_write_b32 v2, v1
	v_mov_b32_e32 v2, 0x27030
	ds_write_b32 v2, v1
	s_or_b64 exec, exec, s[6:7]
	v_cmp_gt_u32_e64 s[6:7], 64, v0
	v_mbcnt_lo_u32_b32 v1, -1, 0
	s_waitcnt lgkmcnt(0)
	s_barrier
	s_and_saveexec_b64 s[8:9], s[6:7]
	s_cbranch_execz .LBB1_9
	v_mov_b32_e32 v2, 0x10410
	v_lshl_add_u32 v3, v0, 4, v2
	ds_read_b128 v[8:11], v3
	s_waitcnt lgkmcnt(0)
	v_add_u32_e32 v7, v9, v8
	v_add3_u32 v7, v7, v10, v11
	v_mov_b32_e32 v2, v7
	s_nop 1
	v_add_u32_dpp v2, v2, v2 row_shr:1 row_mask:0xf bank_mask:0xf
	s_nop 1
	v_add_u32_dpp v2, v2, v2 row_shr:2 row_mask:0xf bank_mask:0xf
	s_nop 1
	v_add_u32_dpp v2, v2, v2 row_shr:4 row_mask:0xf bank_mask:0xf
	s_nop 1
	v_add_u32_dpp v2, v2, v2 row_shr:8 row_mask:0xf bank_mask:0xf
	s_nop 1
	v_add_u32_dpp v2, v2, v2 row_bcast:15 row_mask:0xa bank_mask:0xf
	s_nop 1
	v_add_u32_dpp v2, v2, v2 row_bcast:31 row_mask:0xc bank_mask:0xf
	v_sub_u32_e32 v12, v2, v7
	v_add_u32_e32 v13, v12, v8
	v_add_u32_e32 v14, v13, v9
	v_add_u32_e32 v15, v14, v10
	v_cmp_eq_u32_e32 vcc, 63, v0
	ds_write_b128 v3, v[12:15]
	s_and_b64 exec, exec, vcc
	v_mov_b32_e32 v3, 0x10810
	ds_write_b32 v3, v2

.LBB1_17:
	s_load_dwordx2 s[26:27], s[0:1], 0x10
	s_movk_i32 s3, 0x1000
	s_and_b64 vcc, exec, s[8:9]
	v_cmp_lt_i32_e64 s[8:9], v0, v77
	s_cbranch_vccz .LBB1_40
	s_load_dwordx2 s[44:45], s[0:1], 0x20
	v_or_b32_e32 v113, 0x400, v0
	v_or_b32_e32 v114, 0x800, v0
	v_or_b32_e32 v115, 0xc00, v0
	v_mov_b32_e32 v116, 0x10c20
	v_mov_b32_e32 v117, 0x10c20
	v_mov_b32_e32 v118, 0x10c20
	v_mov_b32_e32 v119, 0x10c20
	v_add_u32_e32 v120, 256, v116
	v_add_u32_e32 v121, 256, v117
	v_add_u32_e32 v122, 256, v118
	v_add_u32_e32 v123, 256, v119
	ds_read_b32 v124, v120
	ds_read_b32 v125, v121
	ds_read_b32 v126, v122
	ds_read_b32 v127, v123
	s_waitcnt lgkmcnt(0)
	v_cmp_le_i32_e64 s[36:37], v124, v0
	v_cmp_le_i32_e64 s[38:39], v125, v113
	v_cmp_le_i32_e64 s[40:41], v126, v114
	v_cmp_le_i32_e64 s[42:43], v127, v115
	v_cndmask_b32_e64 v116, v116, v120, s[36:37]
	v_cndmask_b32_e64 v117, v117, v121, s[38:39]
	v_cndmask_b32_e64 v118, v118, v122, s[40:41]
	v_cndmask_b32_e64 v119, v119, v123, s[42:43]
	v_add_u32_e32 v120, 128, v116
	v_add_u32_e32 v121, 128, v117
	v_add_u32_e32 v122, 128, v118
	v_add_u32_e32 v123, 128, v119
	ds_read_b32 v124, v120
	ds_read_b32 v125, v121
	ds_read_b32 v126, v122
	ds_read_b32 v127, v123
	s_waitcnt lgkmcnt(0)
	v_cmp_le_i32_e64 s[36:37], v124, v0
	v_cmp_le_i32_e64 s[38:39], v125, v113
	v_cmp_le_i32_e64 s[40:41], v126, v114
	v_cmp_le_i32_e64 s[42:43], v127, v115
	v_cndmask_b32_e64 v116, v116, v120, s[36:37]
	v_cndmask_b32_e64 v117, v117, v121, s[38:39]
	v_cndmask_b32_e64 v118, v118, v122, s[40:41]
	v_cndmask_b32_e64 v119, v119, v123, s[42:43]
	v_add_u32_e32 v120, 64, v116
	v_add_u32_e32 v121, 64, v117
	v_add_u32_e32 v122, 64, v118
	v_add_u32_e32 v123, 64, v119
	ds_read_b32 v124, v120
	ds_read_b32 v125, v121
	ds_read_b32 v126, v122
	ds_read_b32 v127, v123
	s_waitcnt lgkmcnt(0)
	v_cmp_le_i32_e64 s[36:37], v124, v0
	v_cmp_le_i32_e64 s[38:39], v125, v113
	v_cmp_le_i32_e64 s[40:41], v126, v114
	v_cmp_le_i32_e64 s[42:43], v127, v115
	v_cndmask_b32_e64 v116, v116, v120, s[36:37]
	v_cndmask_b32_e64 v117, v117, v121, s[38:39]
	v_cndmask_b32_e64 v118, v118, v122, s[40:41]
	v_cndmask_b32_e64 v119, v119, v123, s[42:43]
	v_add_u32_e32 v120, 32, v116
	v_add_u32_e32 v121, 32, v117
	v_add_u32_e32 v122, 32, v118
	v_add_u32_e32 v123, 32, v119
	ds_read_b32 v124, v120
	ds_read_b32 v125, v121
	ds_read_b32 v126, v122
	ds_read_b32 v127, v123
	s_waitcnt lgkmcnt(0)
	v_cmp_le_i32_e64 s[36:37], v124, v0
	v_cmp_le_i32_e64 s[38:39], v125, v113
	v_cmp_le_i32_e64 s[40:41], v126, v114
	v_cmp_le_i32_e64 s[42:43], v127, v115
	v_cndmask_b32_e64 v116, v116, v120, s[36:37]
	v_cndmask_b32_e64 v117, v117, v121, s[38:39]
	v_cndmask_b32_e64 v118, v118, v122, s[40:41]
	v_cndmask_b32_e64 v119, v119, v123, s[42:43]
	v_add_u32_e32 v120, 16, v116
	v_add_u32_e32 v121, 16, v117
	v_add_u32_e32 v122, 16, v118
	v_add_u32_e32 v123, 16, v119
	ds_read_b32 v124, v120
	ds_read_b32 v125, v121
	ds_read_b32 v126, v122
	ds_read_b32 v127, v123
	s_waitcnt lgkmcnt(0)
	v_cmp_le_i32_e64 s[36:37], v124, v0
	v_cmp_le_i32_e64 s[38:39], v125, v113
	v_cmp_le_i32_e64 s[40:41], v126, v114
	v_cmp_le_i32_e64 s[42:43], v127, v115
	v_cndmask_b32_e64 v116, v116, v120, s[36:37]
	v_cndmask_b32_e64 v117, v117, v121, s[38:39]
	v_cndmask_b32_e64 v118, v118, v122, s[40:41]
	v_cndmask_b32_e64 v119, v119, v123, s[42:43]
	v_add_u32_e32 v120, 8, v116
	v_add_u32_e32 v121, 8, v117
	v_add_u32_e32 v122, 8, v118
	v_add_u32_e32 v123, 8, v119
	ds_read_b32 v124, v120
	ds_read_b32 v125, v121
	ds_read_b32 v126, v122
	ds_read_b32 v127, v123
	s_waitcnt lgkmcnt(0)
	v_cmp_le_i32_e64 s[36:37], v124, v0
	v_cmp_le_i32_e64 s[38:39], v125, v113
	v_cmp_le_i32_e64 s[40:41], v126, v114
	v_cmp_le_i32_e64 s[42:43], v127, v115
	v_cndmask_b32_e64 v116, v116, v120, s[36:37]
	v_cndmask_b32_e64 v117, v117, v121, s[38:39]
	v_cndmask_b32_e64 v118, v118, v122, s[40:41]
	v_cndmask_b32_e64 v119, v119, v123, s[42:43]
	v_add_u32_e32 v120, 4, v116
	v_add_u32_e32 v121, 4, v117
	v_add_u32_e32 v122, 4, v118
	v_add_u32_e32 v123, 4, v119
	ds_read_b32 v124, v120
	ds_read_b32 v125, v121
	ds_read_b32 v126, v122
	ds_read_b32 v127, v123
	s_waitcnt lgkmcnt(0)
	v_cmp_le_i32_e64 s[36:37], v124, v0
	v_cmp_le_i32_e64 s[38:39], v125, v113
	v_cmp_le_i32_e64 s[40:41], v126, v114
	v_cmp_le_i32_e64 s[42:43], v127, v115
	v_cndmask_b32_e64 v116, v116, v120, s[36:37]
	v_cndmask_b32_e64 v117, v117, v121, s[38:39]
	v_cndmask_b32_e64 v118, v118, v122, s[40:41]
	v_cndmask_b32_e64 v119, v119, v123, s[42:43]
	ds_read_b32 v120, v116
	ds_read_b32 v121, v117
	ds_read_b32 v122, v118
	ds_read_b32 v123, v119
	ds_read_b32 v124, v116 offset:528
	ds_read_b32 v125, v117 offset:528
	ds_read_b32 v126, v118 offset:528
	ds_read_b32 v127, v119 offset:528
	v_cmp_lt_i32_e64 s[10:11], v114, v77
	v_cmp_lt_i32_e64 s[12:13], v115, v77
	s_waitcnt lgkmcnt(0)
	v_add_u32_e32 v124, v124, v0
	v_add_u32_e32 v125, v125, v113
	v_add_u32_e32 v126, v126, v114
	v_add_u32_e32 v127, v127, v115
	v_sub_u32_e32 v116, v124, v120
	v_sub_u32_e32 v118, v125, v121
	v_sub_u32_e32 v120, v126, v122
	v_sub_u32_e32 v122, v127, v123
	v_ashrrev_i32_e32 v117, 31, v116
	v_ashrrev_i32_e32 v119, 31, v118
	v_ashrrev_i32_e32 v121, 31, v120
	v_ashrrev_i32_e32 v123, 31, v122
	v_lshl_add_u64 v[116:117], v[116:117], 3, s[24:25]
	v_lshl_add_u64 v[118:119], v[118:119], 3, s[24:25]
	v_lshl_add_u64 v[120:121], v[120:121], 3, s[24:25]
	v_lshl_add_u64 v[122:123], v[122:123], 3, s[24:25]
	v_cmp_lt_i32_e32 vcc, v113, v77
	s_mov_b64 s[16:17], exec
	s_and_b64 exec, s[16:17], s[8:9]
	global_load_dwordx2 v[42:43], v[116:117], off
	s_and_b64 exec, s[16:17], vcc
	global_load_dwordx2 v[44:45], v[118:119], off
	s_and_b64 exec, s[16:17], s[10:11]
	global_load_dwordx2 v[46:47], v[120:121], off
	s_and_b64 exec, s[16:17], s[12:13]
	global_load_dwordx2 v[48:49], v[122:123], off
	s_mov_b64 exec, s[16:17]
	v_lshrrev_b32_e32 v116, 6, v0
	s_mul_i32 s39, s2, 0x18800
	v_and_b32_e32 v118, 63, v0
	v_readfirstlane_b32 s38, v116
	v_lshlrev_b32_e32 v118, 4, v118
	v_mov_b32_e32 v119, 0
	s_add_i32 s38, s38, 44
	s_add_u32 s36, s44, s39
	s_addc_u32 s37, s45, 0
.Lq_dma2_loop:
	s_lshl_b32 s40, s38, 10
	s_add_u32 s42, s36, s40
	s_addc_u32 s43, s37, 0
	s_add_i32 s41, s40, 69680
	v_lshl_add_u64 v[120:121], s[42:43], 0, v[118:119]
	s_mov_b32 m0, s41
	s_add_i32 s38, s38, 16
	global_load_lds_dwordx4 v[120:121], off
	s_cmp_lt_u32 s38, 88
	s_cbranch_scc1 .Lq_dma2_loop

.LBB1_38:
	s_waitcnt vmcnt(2)
	v_lshrrev_b32_e32 v5, 18, v48
	v_and_b32_e32 v5, 0x3ffc, v5
	v_add_u32_e32 v5, 0x10820, v5
	v_mov_b32_e32 v7, 1
	ds_add_rtn_u32 v5, v5, v7

.LBB1_119:
	s_and_b64 vcc, exec, s[0:1]
	s_cbranch_vccz .LBB1_189
	v_cmp_lt_i32_e32 vcc, v0, v77
	s_and_saveexec_b64 s[0:1], vcc
	s_cbranch_execz .LBB1_122
	s_waitcnt vmcnt(2) lgkmcnt(0)
	v_lshrrev_b32_e32 v6, 18, v42
	v_and_b32_e32 v6, 0x3ffc, v6
	v_or_b32_e32 v6, 0x10000, v6
	ds_read_b32 v6, v6
	v_lshlrev_b32_e32 v2, 3, v2
	v_and_b32_e32 v42, 0xfffff, v42
	s_waitcnt lgkmcnt(0)
	v_lshl_add_u32 v2, v6, 3, v2
	ds_write_b64 v2, v[42:43] offset:32768
.LBB1_122:
	s_or_b64 exec, exec, s[0:1]
	v_or_b32_e32 v2, 0x400, v0
	v_cmp_lt_i32_e32 vcc, v2, v77
	s_and_saveexec_b64 s[0:1], vcc
	s_cbranch_execz .LBB1_124
	s_waitcnt vmcnt(2)
	v_lshrrev_b32_e32 v2, 18, v44
	v_and_b32_e32 v2, 0x3ffc, v2
	v_or_b32_e32 v2, 0x10000, v2
	ds_read_b32 v2, v2
	v_lshlrev_b32_e32 v3, 3, v3
	v_and_b32_e32 v44, 0xfffff, v44
	s_waitcnt lgkmcnt(0)
	v_lshl_add_u32 v2, v2, 3, v3
	ds_write_b64 v2, v[44:45] offset:32768
.LBB1_124:
	s_or_b64 exec, exec, s[0:1]
	v_or_b32_e32 v2, 0x800, v0
	v_cmp_lt_i32_e32 vcc, v2, v77
	s_and_saveexec_b64 s[0:1], vcc
	s_cbranch_execz .LBB1_126
	s_waitcnt vmcnt(2)
	v_lshrrev_b32_e32 v2, 18, v46
	v_and_b32_e32 v2, 0x3ffc, v2
	v_or_b32_e32 v2, 0x10000, v2
	ds_read_b32 v2, v2
	v_lshlrev_b32_e32 v3, 3, v4
	v_and_b32_e32 v46, 0xfffff, v46
	s_waitcnt lgkmcnt(0)
	v_lshl_add_u32 v2, v2, 3, v3
	ds_write_b64 v2, v[46:47] offset:32768
.LBB1_126:
	s_or_b64 exec, exec, s[0:1]
	v_or_b32_e32 v2, 0xc00, v0
	v_cmp_lt_i32_e32 vcc, v2, v77
	s_and_saveexec_b64 s[0:1], vcc
	s_cbranch_execz .LBB1_128
	s_waitcnt vmcnt(2)
	v_lshrrev_b32_e32 v2, 18, v48
	v_and_b32_e32 v2, 0x3ffc, v2
	v_or_b32_e32 v2, 0x10000, v2
	ds_read_b32 v2, v2
	v_lshlrev_b32_e32 v3, 3, v5
	v_and_b32_e32 v48, 0xfffff, v48
	s_waitcnt lgkmcnt(0)
	v_lshl_add_u32 v2, v2, 3, v3
	ds_write_b64 v2, v[48:49] offset:32768
.LBB1_128:
	s_or_b64 exec, exec, s[0:1]
	v_and_b32_e32 v4, 15, v0
	v_mov_b32_e32 v3, 0
	v_lshlrev_b32_e32 v2, 5, v4
	v_lshlrev_b32_e32 v4, 4, v4
	v_mov_b32_e32 v5, v3
	v_bfe_u32 v59, v0, 4, 2
	v_lshl_add_u64 v[40:41], s[20:21], 0, v[4:5]
	v_and_b32_e32 v4, 1, v0
	s_waitcnt lgkmcnt(0)
	v_lshlrev_b32_e32 v6, 1, v0
	v_and_b32_e32 v36, 63, v0
	v_lshl_add_u64 v[38:39], s[18:19], 0, v[2:3]
	v_cmp_eq_u32_e64 s[2:3], 1, v4
	v_and_b32_e32 v4, 28, v6
	s_waitcnt vmcnt(2)
	v_lshl_add_u64 v[44:45], s[22:23], 0, v[2:3]
	v_and_b32_e32 v2, 7, v0
	v_bitop3_b32 v69, v0, 63, v0 bitop3:0x3f
	v_lshlrev_b32_e32 v70, 11, v86
	v_lshlrev_b32_e32 v0, 5, v59
	v_mbcnt_hi_u32_b32 v75, -1, v1
	v_lshlrev_b32_e32 v2, 2, v2
	v_or3_b32 v71, v70, v0, v4
	v_lshlrev_b32_e32 v72, 2, v36
	v_and_b32_e32 v0, 64, v75
	s_barrier
	v_cmp_eq_u32_e64 s[0:1], 0, v36
	v_lshl_add_u64 v[42:43], s[8:9], 0, v[4:5]
	v_cmp_gt_u32_e64 s[4:5], 16, v36
	v_and_b32_e32 v68, 14, v6
	v_lshl_add_u64 v[46:47], s[8:9], 0, v[2:3]
	v_or_b32_e32 v37, 64, v36
	v_or_b32_e32 v73, v70, v72
	v_mov_b32_e32 v74, 0x10408
	s_mov_b32 s14, 0x3fffffc0
	v_add_u32_e32 v76, 64, v0
	v_xor_b32_e32 v77, 1, v75
	v_mov_b32_e32 v78, 0x8004
	v_xor_b32_e32 v79, 16, v75
	v_xor_b32_e32 v80, 32, v75
	v_and_b32_e32 v112, 15, v36
	v_lshlrev_b32_e32 v112, 5, v112
	v_mov_b32_e32 v114, 0x27030
	v_cmp_eq_u32_e32 vcc, 0, v36
	s_mov_b32 s46, 1
	s_nop 1
	v_cndmask_b32_e64 v115, 0, 1, vcc
	s_branch .LBB1_133

.LBB1_131:
	s_cmp_eq_u32 s46, 0
	s_cbranch_scc1 .Lq_nosig
	s_waitcnt vmcnt(0)
	ds_add_u32 v114, v115
	s_mov_b32 s46, 0

.LBB1_133:
	s_waitcnt lgkmcnt(0)
	ds_read_b32 v113, v114
	v_mov_b32_e32 v0, 0
	s_and_saveexec_b64 s[6:7], s[0:1]
	s_cbranch_execz .LBB1_137
	s_mov_b64 s[10:11], exec
	v_mbcnt_lo_u32_b32 v0, s10, 0
	v_mbcnt_hi_u32_b32 v0, s11, v0
	v_cmp_eq_u32_e32 vcc, 0, v0
	s_and_saveexec_b64 s[8:9], vcc
	s_bcnt1_i32_b64 s10, s[10:11]
	v_mov_b32_e32 v1, s10
	ds_add_rtn_u32 v1, v74, v1
	s_or_b64 exec, exec, s[8:9]
	s_waitcnt lgkmcnt(0)
	v_readfirstlane_b32 s8, v1
	s_nop 1
	v_add_u32_e32 v0, s8, v0
.LBB1_137:
	s_or_b64 exec, exec, s[6:7]
	v_readfirstlane_b32 s10, v0
	s_cmp_ge_i32 s10, s28
	s_mov_b64 s[6:7], -1
	s_cbranch_scc1 .LBB1_132
	s_add_i32 s8, s10, s29
	s_ashr_i32 s9, s8, 31
	s_waitcnt lgkmcnt(0)
	v_readfirstlane_b32 s45, v113
	s_cmp_lt_u32 s10, 88
	s_cbranch_scc1 .Lq_lds
	s_cmp_lt_u32 s10, 176
	s_cbranch_scc0 .Lq_glob
	s_cmp_eq_u32 s45, 16
	s_cbranch_scc0 .Lq_glob
.Lq_lds:
	s_lshl_b32 s6, s10, 9
	s_add_i32 s6, s6, 69680
	v_add_u32_e32 v8, s6, v112
	ds_read_b128 v[0:3], v8
	ds_read_b128 v[4:7], v8 offset:16
	s_branch .Lq_done

.LBB1_190:
	s_waitcnt vmcnt(2)
	v_lshrrev_b32_e32 v3, 18, v42
	v_and_b32_e32 v3, 0x3ffc, v3
	v_add_u32_e32 v3, 0x10820, v3
	v_mov_b32_e32 v4, 1
	ds_add_rtn_u32 v8, v3, v4
	v_mov_b32_e32 v9, v2
	v_mov_b32_e32 v10, v2
	v_mov_b32_e32 v11, v2
	s_waitcnt lgkmcnt(0)
	v_mov_b64_e32 v[2:3], v[8:9]
	v_mov_b64_e32 v[4:5], v[10:11]
	s_or_b64 exec, exec, s[16:17]
	s_and_saveexec_b64 s[8:9], vcc
	s_cbranch_execz .LBB1_36
.LBB1_191:
	s_waitcnt vmcnt(2)
	v_lshrrev_b32_e32 v3, 18, v44
	v_and_b32_e32 v3, 0x3ffc, v3
	v_add_u32_e32 v3, 0x10820, v3
	v_mov_b32_e32 v7, 1
	ds_add_rtn_u32 v3, v3, v7
	s_or_b64 exec, exec, s[8:9]
	s_and_saveexec_b64 s[8:9], s[10:11]
	s_cbranch_execz .LBB1_37
.LBB1_192:
	s_waitcnt vmcnt(2)
	v_lshrrev_b32_e32 v4, 18, v46
	v_and_b32_e32 v4, 0x3ffc, v4
	v_add_u32_e32 v4, 0x10820, v4
	v_mov_b32_e32 v7, 1
	ds_add_rtn_u32 v4, v4, v7
	s_or_b64 exec, exec, s[8:9]
	s_and_saveexec_b64 s[8:9], s[12:13]
	s_cbranch_execnz .LBB1_38
	s_branch .LBB1_39

	.amdhsa_kernel _Z11edge_kernelPK15HIP_vector_typeIjLj2EEPKiPiPS_IiLj2EEPKfPK6__halfPfSD_
		.amdhsa_group_segment_fixed_size 159808
		.amdhsa_private_segment_fixed_size 0
		.amdhsa_kernarg_size 64
		.amdhsa_user_sgpr_count 2
		.amdhsa_user_sgpr_dispatch_ptr 0
		.amdhsa_user_sgpr_queue_ptr 0
		.amdhsa_user_sgpr_kernarg_segment_ptr 1
		.amdhsa_user_sgpr_dispatch_id 0
		.amdhsa_user_sgpr_kernarg_preload_length 0
		.amdhsa_user_sgpr_kernarg_preload_offset 0
		.amdhsa_user_sgpr_private_segment_size 0
		.amdhsa_uses_dynamic_stack 0
		.amdhsa_enable_private_segment 0
		.amdhsa_system_sgpr_workgroup_id_x 1
		.amdhsa_system_sgpr_workgroup_id_y 0
		.amdhsa_system_sgpr_workgroup_id_z 0
		.amdhsa_system_sgpr_workgroup_info 0
		.amdhsa_system_vgpr_workitem_id 0
		.amdhsa_next_free_vgpr 128
		.amdhsa_next_free_sgpr 48
		.amdhsa_accum_offset 128
		.amdhsa_reserve_vcc 1
		.amdhsa_float_round_mode_32 0
		.amdhsa_float_round_mode_16_64 0
		.amdhsa_float_denorm_mode_32 3
		.amdhsa_float_denorm_mode_16_64 3
		.amdhsa_dx10_clamp 1
		.amdhsa_ieee_mode 1
		.amdhsa_fp16_overflow 0
		.amdhsa_tg_split 0
		.amdhsa_exception_fp_ieee_invalid_op 0
		.amdhsa_exception_fp_denorm_src 0
		.amdhsa_exception_fp_ieee_div_zero 0
		.amdhsa_exception_fp_ieee_overflow 0
		.amdhsa_exception_fp_ieee_underflow 0
		.amdhsa_exception_fp_ieee_inexact 0
		.amdhsa_exception_int_div_zero 0
	.end_amdhsa_kernel

amdhsa.kernels:
  - .agpr_count:     0
    .args:
      - .actual_access:  read_only
        .address_space:  global
        .offset:         0
        .size:           8
        .value_kind:     global_buffer
      - .actual_access:  read_only
        .address_space:  global
        .offset:         8
        .size:           8
        .value_kind:     global_buffer
      - .actual_access:  write_only
        .address_space:  global
        .offset:         16
        .size:           8
        .value_kind:     global_buffer
      - .actual_access:  write_only
        .address_space:  global
        .offset:         24
        .size:           8
        .value_kind:     global_buffer
      - .actual_access:  write_only
        .address_space:  global
        .offset:         32
        .size:           8
        .value_kind:     global_buffer
      - .actual_access:  read_only
        .address_space:  global
        .offset:         40
        .size:           8
        .value_kind:     global_buffer
      - .actual_access:  read_only
        .address_space:  global
        .offset:         48
        .size:           8
        .value_kind:     global_buffer
      - .actual_access:  read_only
        .address_space:  global
        .offset:         56
        .size:           8
        .value_kind:     global_buffer
      - .actual_access:  read_only
        .address_space:  global
        .offset:         64
        .size:           8
        .value_kind:     global_buffer
      - .actual_access:  write_only
        .address_space:  global
        .offset:         72
        .size:           8
        .value_kind:     global_buffer
      - .actual_access:  write_only
        .address_space:  global
        .offset:         80
        .size:           8
        .value_kind:     global_buffer
    .group_segment_fixed_size: 72704
    .kernarg_segment_align: 8
    .kernarg_segment_size: 88
    .language:       OpenCL C
    .language_version:
      - 2
      - 0
    .max_flat_workgroup_size: 512
    .name:           _Z9l1_kernelPKiS0_P15HIP_vector_typeIjLj2EEPiS4_PKfS6_S6_S6_PfP6__half
    .private_segment_fixed_size: 0
    .sgpr_count:     76
    .sgpr_spill_count: 0
    .symbol:         _Z9l1_kernelPKiS0_P15HIP_vector_typeIjLj2EEPiS4_PKfS6_S6_S6_PfP6__half.kd
    .uniform_work_group_size: 1
    .uses_dynamic_stack: false
    .vgpr_count:     252
    .vgpr_spill_count: 0
    .wavefront_size: 64
  - .agpr_count:     0
    .args:
      - .actual_access:  read_only
        .address_space:  global
        .offset:         0
        .size:           8
        .value_kind:     global_buffer
      - .actual_access:  read_only
        .address_space:  global
        .offset:         8
        .size:           8
        .value_kind:     global_buffer
      - .address_space:  global
        .offset:         16
        .size:           8
        .value_kind:     global_buffer
      - .address_space:  global
        .offset:         24
        .size:           8
        .value_kind:     global_buffer
      - .actual_access:  read_only
        .address_space:  global
        .offset:         32
        .size:           8
        .value_kind:     global_buffer
      - .actual_access:  read_only
        .address_space:  global
        .offset:         40
        .size:           8
        .value_kind:     global_buffer
      - .actual_access:  write_only
        .address_space:  global
        .offset:         48
        .size:           8
        .value_kind:     global_buffer
      - .actual_access:  write_only
        .address_space:  global
        .offset:         56
        .size:           8
        .value_kind:     global_buffer
    .group_segment_fixed_size: 159808
    .kernarg_segment_align: 8
    .kernarg_segment_size: 64
    .language:       OpenCL C
    .language_version:
      - 2
      - 0
    .max_flat_workgroup_size: 1024
    .name:           _Z11edge_kernelPK15HIP_vector_typeIjLj2EEPKiPiPS_IiLj2EEPKfPK6__halfPfSD_
    .private_segment_fixed_size: 0
    .sgpr_count:     54
    .sgpr_spill_count: 0
    .symbol:         _Z11edge_kernelPK15HIP_vector_typeIjLj2EEPKiPiPS_IiLj2EEPKfPK6__halfPfSD_.kd
    .uniform_work_group_size: 1
    .uses_dynamic_stack: false
    .vgpr_count:     128
    .vgpr_spill_count: 0
    .wavefront_size: 64
